# P7 stream prologue: gather-index loads now overlap with the four B-tile LDS-DMA loads (wait moved to first use of the indices)
# speedup vs baseline: 1.0073x; 1.0012x over previous
;     __device__ __forceinline__ bool next(int i, Unit& u) const {
;         if (i >= hi) return false;
;         const int L = i * G + c;
;         const unsigned msk = (unsigned)__ballot(L < pfxU[(fresh_lane() & 31) + 1]);
;         if (msk == 0u) return false;
;         const int e = __builtin_ctz(msk);
;         const int r = L - __builtin_amdgcn_readfirstlane(pfxU[e]), mt = (__builtin_amdgcn_readfirstlane(cnt[e]) + 255) >> 8;
;         u.e = e; u.pn = r / mt; u.pm = r - u.pn * mt; return true;
;     }
;     __device__ __forceinline__ const char* a_base(const Unit& u) const { return GATHER ? A : A + ((size_t)__builtin_amdgcn_readfirstlane(poff[u.e]) + (size_t)u.pm * BM) * ROWB; }
;     __device__ __forceinline__ void a_offs(const Unit& u, const unsigned (&nat)[2], unsigned (&v)[4]) const {
;         if (!GATHER) { v[0] = nat[0]; v[1] = nat[1]; v[2] = nat[0] + Geo<true>::HSTEP; v[3] = nat[1] + Geo<true>::HSTEP; return; }
;         const int n = cnt[u.e];
;         unsigned off[4]; int tok[4];
; #pragma unroll
;         for (int h = 0; h < 2; ++h)
; #pragma unroll
;             for (int i = 0; i < 2; ++i) { int pos = u.pm * BM + h * HALF + (int)(nat[i] / ROWB); pos = pos < n ? pos : n - 1; off[h * 2 + i] = (unsigned)pos * 4u; }
;         asm volatile("global_load_dword %0, %4, %8\n\tglobal_load_dword %1, %5, %8\n\tglobal_load_dword %2, %6, %8\n\tglobal_load_dword %3, %7, %8\n\ts_waitcnt vmcnt(0)"
;                      : "=&v"(tok[0]), "=&v"(tok[1]), "=&v"(tok[2]), "=&v"(tok[3]) : "v"(off[0]), "v"(off[1]), "v"(off[2]), "v"(off[3]), "s"(tokof + (size_t)u.e * ECAP) : "memory");
; #pragma unroll
;         for (int q = 0; q < 4; ++q) v[q] = (unsigned)tok[q] * ROWB + nat[q & 1] % ROWB;
;     }
; template <class Epi, class Sched>
; __device__ __forceinline__ void gemm_phase(LAS unsigned char* lds, const Sched& S, const Epi& E) {
;     const int wid = __builtin_amdgcn_readfirstlane(threadIdx.x >> 6), lane = fresh_lane(), tid = wid * 64 + lane, wr = wid >> 2, wc = wid & 3, fr = lane & 15, fq = lane >> 4;
;     constexpr bool FP8 = Sched::FP8; constexpr unsigned ROWB = Geo<FP8>::ROWB, HSTEP = Geo<FP8>::HSTEP; constexpr int NTK = Geo<FP8>::NTK;
;     unsigned natA[2], voffB[2];
; #pragma unroll
;     for (int i = 0; i < 2; ++i) { int R, C; stage_rc(tid * 16 + i * 8192, R, C); const int Rb = Epi::PERM ? ((R & ~31) + perm32(R & 31)) : R;
.LBB0_995:
	v_readfirstlane_b32 s2, v0
	v_mov_b32_e32 v2, v1
	s_cmp_ge_i32 s25, s87
	s_cbranch_scc1 .LBB0_768
	v_mov_b32_e32 v3, v1
	s_mul_i32 s0, s25, s33
	v_and_b32_e32 v3, 31, v3
	v_lshl_add_u32 v3, v3, 2, s97
	ds_read_b32 v3, v3 offset:4
	v_readlane_b32 s1, v253, 5
	s_add_i32 s0, s0, s1
	s_waitcnt lgkmcnt(0)
	v_cmp_lt_i32_e32 vcc, s0, v3
	s_cmp_eq_u32 vcc_lo, 0
	s_cbranch_scc1 .LBB0_768
	s_and_b32 s1, s2, 0xffffffc0
	v_add_u32_e32 v3, s1, v2
	v_ashrrev_i32_e32 v5, 31, v3
	v_lshrrev_b32_e32 v5, 26, v5
	v_lshlrev_b32_e32 v4, 4, v3
	v_add_u32_e32 v5, v3, v5
	v_bfe_i32 v3, v3, 27, 1
	v_lshrrev_b32_e32 v3, 22, v3
	v_add_u32_e32 v3, v4, v3
	v_and_b32_e32 v3, 0xfffffc00, v3
	v_sub_u32_e32 v3, v4, v3
	v_lshrrev_b32_e32 v6, 4, v3
	v_bitop3_b32 v3, v6, v3, 32 bitop3:0x6c
	v_ashrrev_i32_e32 v7, 31, v3
	v_lshrrev_b32_e32 v7, 26, v7
	v_ashrrev_i32_e32 v5, 6, v5
	v_add_u32_e32 v7, v3, v7
	v_lshlrev_b32_e32 v6, 3, v5
	v_ashrrev_i32_e32 v8, 6, v7
	v_and_b32_e32 v7, 0xc0, v7
	v_and_b32_e32 v6, -16, v6
	v_lshlrev_b32_e32 v5, 5, v5
	v_sub_u32_e32 v3, v3, v7
	v_add_u32_e32 v6, v8, v6
	v_and_b32_e32 v5, 32, v5
	v_ashrrev_i16_sdwa v3, v198, sext(v3) dst_sel:DWORD dst_unused:UNUSED_PAD src0_sel:DWORD src1_sel:BYTE_0
	v_add_u32_sdwa v3, v5, sext(v3) dst_sel:DWORD dst_unused:UNUSED_PAD src0_sel:DWORD src1_sel:WORD_0
	v_lshlrev_b32_e32 v5, 1, v6
	v_lshrrev_b32_e32 v7, 2, v6
	v_and_b32_e32 v8, 3, v8
	s_mov_b32 s1, 0x1fffe0
	v_and_b32_e32 v5, 24, v5
	v_and_b32_e32 v7, 4, v7
	v_and_or_b32 v8, v6, s1, v8
	v_or3_b32 v5, v8, v7, v5
	v_lshlrev_b32_e32 v7, 1, v3
	v_add_u32_e32 v4, 0x2000, v4
	v_lshl_add_u32 v194, v5, 11, v7
	v_ashrrev_i32_e32 v5, 31, v4
	v_lshrrev_b32_e32 v5, 22, v5
	v_add_u32_e32 v5, v4, v5
	v_ashrrev_i32_e32 v5, 10, v5
	v_mul_i32_i24_e32 v8, 0x400, v5
	v_sub_u32_e32 v4, v4, v8
	v_lshrrev_b32_e32 v8, 4, v4
	v_bitop3_b32 v4, v8, v4, 32 bitop3:0x6c
	v_ashrrev_i32_e32 v9, 31, v4
	v_lshrrev_b32_e32 v9, 26, v9
	v_add_u32_e32 v9, v4, v9
	v_lshlrev_b32_e32 v8, 3, v5
	v_ashrrev_i32_e32 v10, 6, v9
	v_and_b32_e32 v9, 0xc0, v9
	v_and_b32_e32 v8, -16, v8
	v_lshlrev_b32_e32 v5, 5, v5
	v_sub_u32_e32 v4, v4, v9
	v_add_u32_e32 v8, v10, v8
	v_and_b32_e32 v5, 32, v5
	v_ashrrev_i16_sdwa v4, v198, sext(v4) dst_sel:DWORD dst_unused:UNUSED_PAD src0_sel:DWORD src1_sel:BYTE_0
	v_and_b32_e32 v10, 3, v10
	s_ff1_i32_b32 s52, vcc_lo
	v_add_u32_sdwa v4, v5, sext(v4) dst_sel:DWORD dst_unused:UNUSED_PAD src0_sel:DWORD src1_sel:WORD_0
	v_lshlrev_b32_e32 v5, 1, v8
	v_lshrrev_b32_e32 v9, 2, v8
	v_and_or_b32 v10, v8, s1, v10
	s_lshl_b32 s1, s52, 2
	v_and_b32_e32 v5, 24, v5
	v_and_b32_e32 v9, 4, v9
	s_add_i32 s1, s1, 0
	v_or3_b32 v5, v10, v9, v5
	v_lshlrev_b32_e32 v9, 1, v4
	s_add_i32 s12, s1, 0x20200
	v_lshl_add_u32 v201, v5, 11, v9
	v_mov_b32_e32 v5, s12
	ds_read_b32 v5, v5
	s_add_i32 s1, s1, 0x20100
	s_lshr_b32 s3, s2, 6
	s_lshr_b32 s4, s2, 8
	s_lshl_b32 s5, s3, 10
	s_waitcnt lgkmcnt(0)
	v_readfirstlane_b32 s12, v5
	v_mov_b32_e32 v5, s1
	ds_read_b32 v5, v5
	s_sub_i32 s0, s0, s12
	s_abs_i32 s13, s0
	v_lshrrev_b32_e32 v3, 10, v3
	v_lshrrev_b32_e32 v4, 10, v4
	s_waitcnt lgkmcnt(0)
	v_readfirstlane_b32 s1, v5
	s_addk_i32 s1, 0xff
	s_ashr_i32 s1, s1, 8
	s_abs_i32 s14, s1
	v_cvt_f32_u32_e32 v10, s14
	s_sub_i32 s16, 0, s14
	s_xor_b32 s12, s0, s1
	s_ashr_i32 s12, s12, 31
	v_rcp_iflag_f32_e32 v10, v10
	v_add_u32_e32 v3, v3, v6
	v_add_u32_e32 v4, v4, v8
	v_and_b32_e32 v3, 0x1fffff, v3
	v_mul_f32_e32 v10, 0x4f7ffffe, v10
	v_cvt_u32_f32_e32 v10, v10
	v_and_b32_e32 v4, 0x1fffff, v4
	v_add_u32_e32 v5, -1, v5
	v_and_b32_e32 v202, 0x7fe, v7
	v_readfirstlane_b32 s17, v10
	s_mul_i32 s16, s16, s17
	s_mul_hi_u32 s16, s17, s16
	s_add_i32 s17, s17, s16
	s_mul_hi_u32 s16, s13, s17
	s_mul_i32 s17, s16, s14
	s_sub_i32 s13, s13, s17
	s_add_i32 s17, s16, 1
	s_sub_i32 s22, s13, s14
	s_cmp_ge_u32 s13, s14
	s_cselect_b32 s16, s17, s16
	s_cselect_b32 s13, s22, s13
	s_add_i32 s17, s16, 1
	s_cmp_ge_u32 s13, s14
	s_cselect_b32 s13, s17, s16
	s_xor_b32 s13, s13, s12
	s_sub_i32 s54, s13, s12
	s_mul_i32 s1, s1, s54
	s_sub_i32 s79, s0, s1
	s_lshl_b32 s0, s79, 8
	v_add_u32_e32 v6, s0, v3
	v_add_u32_e32 v8, s0, v4
	s_bitset1_b32 s0, 7
	v_add_u32_e32 v10, s0, v3
	v_add_u32_e32 v11, s0, v4
	s_lshl_b32 s0, s52, 15
	s_add_u32 s0, s83, s0
	v_min_i32_e32 v6, v6, v5
	v_min_i32_e32 v8, v8, v5
	v_min_i32_e32 v10, v10, v5
	v_min_i32_e32 v5, v11, v5
	s_addc_u32 s1, s86, 0
	s_ashr_i32 s55, s54, 31
	v_lshlrev_b32_e32 v6, 2, v6
	v_lshlrev_b32_e32 v8, 2, v8
	v_lshlrev_b32_e32 v10, 2, v10
	v_lshlrev_b32_e32 v5, 2, v5
	global_load_dword v11, v6, s[0:1]
	global_load_dword v12, v8, s[0:1]
	global_load_dword v13, v10, s[0:1]
	global_load_dword v14, v5, s[0:1]
	s_lshl_b32 s12, s52, 23
	s_lshl_b64 s[0:1], s[54:55], 19
	s_add_u32 s12, s81, s12
	s_addc_u32 s13, s82, 0
	s_add_u32 s58, s12, s0
	s_addc_u32 s59, s13, s1
	s_add_i32 s29, s5, 0
	s_add_i32 s30, s29, 0x10000
	s_mov_b32 s0, m0
	s_mov_b32 m0, s30
	s_nop 0
	global_load_lds_dwordx4 v194, s[58:59]
	s_mov_b32 m0, s0
	s_add_i32 s31, s29, 0x12000
	s_mov_b32 s0, m0
	s_mov_b32 m0, s31
	s_nop 0
	global_load_lds_dwordx4 v201, s[58:59]
	s_mov_b32 m0, s0
	s_add_u32 s0, s58, 0x40000
	s_addc_u32 s1, s59, 0
	s_add_i32 s36, s29, 0x14000
	s_mov_b32 s5, m0
	s_mov_b32 m0, s36
	s_nop 0
	global_load_lds_dwordx4 v194, s[0:1]
	s_mov_b32 m0, s5
	s_add_i32 s55, s29, 0x16000
	s_mov_b32 s5, m0
	s_mov_b32 m0, s55
	s_nop 0
	global_load_lds_dwordx4 v201, s[0:1]
	s_mov_b32 m0, s5
	s_waitcnt vmcnt(4)
	v_lshl_or_b32 v204, v11, 11, v202
	v_and_b32_e32 v203, 0x7fe, v9
	s_mov_b32 s0, m0
	s_mov_b32 m0, s29
	s_nop 0
	global_load_lds_dwordx4 v204, s[18:19]
	s_mov_b32 m0, s0
	v_lshl_or_b32 v205, v12, 11, v203
	s_add_i32 s85, s29, 0x2000
	s_mov_b32 s0, m0
	s_mov_b32 m0, s85
	s_nop 0
	global_load_lds_dwordx4 v205, s[18:19]
	s_mov_b32 m0, s0
	v_lshl_or_b32 v206, v13, 11, v202
	s_add_i32 s16, s29, 0x4000
	s_mov_b32 s0, m0
	s_mov_b32 m0, s16
	s_nop 0
	global_load_lds_dwordx4 v206, s[18:19]
	s_mov_b32 m0, s0
	v_lshl_or_b32 v207, v14, 11, v203
	s_add_i32 s17, s29, 0x6000
	s_mov_b32 s0, m0
	s_mov_b32 m0, s17
	s_nop 0
	global_load_lds_dwordx4 v207, s[18:19]
	s_mov_b32 m0, s0
	s_cmp_eq_u32 s4, 1
	s_cselect_b64 s[0:1], -1, 0
	s_cmp_lg_u32 s4, 1
	s_cbranch_scc1 .LBB0_999
	s_barrier
